# HGRN2 scan loop converts 896 W1 tiles in its shadow (quad-DPP transpose, 4 loads per wave per chunk); GEMM-in epilogue conversion removed
# baseline (speedup 1.0000x reference)
.LBB0_86:
	s_cmp_lt_i32 s50, 2
	s_cselect_b64 s[6:7], -1, 0
	s_and_b64 s[0:1], s[6:7], s[2:3]
	s_andn2_b64 vcc, exec, s[0:1]
	v_writelane_b32 v254, s60, 4
	s_cbranch_vccnz .LBB0_260
	s_mov_b64 s[2:3], s[80:81]
	s_load_dwordx2 s[8:9], s[2:3], 0xa8
	s_cmpk_lg_i32 s56, 0x100
	s_cselect_b32 s0, s56, 0xc8
	s_cmp_ge_i32 s78, s0
	s_mov_b64 s[4:5], -1
	s_cbranch_scc0 .LBB0_145
	s_sub_i32 s1, s78, s0
	s_cmpk_gt_i32 s1, 0x177f
	s_cbranch_scc1 .LBB0_144
	s_sub_i32 s20, s56, s0
	s_abs_i32 s4, s20
	v_cvt_f32_u32_e32 v1, s4
	s_load_dwordx2 s[10:11], s[2:3], 0x78
	s_load_dwordx2 s[12:13], s[2:3], 0x88
	s_sub_i32 s2, s20, s1
	s_add_i32 s3, s2, 0x177f
	v_rcp_iflag_f32_e32 v1, v1
	s_sub_i32 s2, 0xffffe881, s2
	s_xor_b32 s14, s3, s20
	s_sub_i32 s5, 0, s4
	v_mul_f32_e32 v1, 0x4f7ffffe, v1
	v_cvt_u32_f32_e32 v1, v1
	s_max_i32 s2, s3, s2
	s_ashr_i32 s3, s14, 31
	v_readfirstlane_b32 s14, v1
	s_mul_i32 s5, s5, s14
	s_mul_hi_u32 s5, s14, s5
	s_add_i32 s14, s14, s5
	s_mul_hi_u32 s5, s2, s14
	s_mul_i32 s14, s5, s4
	s_sub_i32 s2, s2, s14
	s_add_i32 s14, s5, 1
	s_sub_i32 s15, s2, s4
	s_cmp_ge_u32 s2, s4
	s_cselect_b32 s5, s14, s5
	s_cselect_b32 s2, s15, s2
	s_add_i32 s14, s5, 1
	s_cmp_ge_u32 s2, s4
	s_cselect_b32 s2, s14, s5
	s_xor_b32 s2, s2, s3
	s_sub_i32 s29, s2, s3
	s_lshl_b32 s21, s29, 2
	s_add_i32 s22, s21, -1
	s_cmp_gt_i32 s29, 0
	s_cselect_b64 s[2:3], -1, 0
	s_and_b64 s[4:5], s[2:3], exec
	s_cselect_b32 s18, 0, s22
	s_ashr_i32 s4, s18, 2
	s_mul_i32 s17, s4, s20
	s_add_i32 s17, s17, s1
	s_cmpk_gt_i32 s17, 0x1fff
	s_mov_b32 s5, 0
	s_cbranch_scc0 .LBB0_91
	s_add_i32 s4, s17, 0xffffe000
	s_lshr_b32 s4, s4, 7
	s_lshl_b64 s[4:5], s[4:5], 24
	s_waitcnt lgkmcnt(0)
	s_add_u32 s14, s12, s4
	s_addc_u32 s15, s13, s5
	s_lshl_b32 s4, s17, 4
	s_and_b32 s26, s4, 0x780
	s_lshl_b32 s4, s17, 8
	s_and_b32 s16, s4, 0x700
	s_mov_b64 s[4:5], 0x800
	s_cbranch_execz .LBB0_92
	s_branch .LBB0_93

.LBB0_354:
	v_add_u32_e32 v8, 0x200, v8
	s_movk_i32 s70, 0x1fff
	v_cmp_lt_u32_e32 vcc, s70, v8
	ds_write_b32 v7, v69
	s_or_b64 s[58:59], vcc, s[58:59]
	v_add_u32_e32 v7, 0x800, v7
	s_andn2_b64 exec, exec, s[58:59]
	s_cbranch_execnz .LBB0_354
	s_or_b64 exec, exec, s[58:59]
	s_waitcnt vmcnt(0)
	v_sub_f32_e32 v4, v4, v2
	v_mul_f32_e32 v2, 0x3fb8aa3b, v4
	s_mov_b32 s46, 0x3fb8aa3b
	v_fma_f32 v7, v4, s46, -v2
	v_rndne_f32_e32 v8, v2
	v_fmac_f32_e32 v7, 0x32a5705f, v4
	v_sub_f32_e32 v2, v2, v8
	v_add_f32_e32 v2, v2, v7
	v_cvt_i32_f32_e32 v7, v8
	v_exp_f32_e32 v2, v2
	v_sub_f32_e32 v3, v5, v3
	s_and_b64 s[58:59], s[40:41], exec
	v_readlane_b32 s58, v254, 15
	v_ldexp_f32 v7, v2, v7
	v_mul_f32_e32 v2, 0x3fb8aa3b, v3
	v_fma_f32 v5, v3, s46, -v2
	v_rndne_f32_e32 v8, v2
	v_fmac_f32_e32 v5, 0x32a5705f, v3
	v_sub_f32_e32 v2, v2, v8
	v_add_f32_e32 v2, v2, v5
	v_exp_f32_e32 v5, v2
	v_cvt_i32_f32_e32 v8, v8
	s_mov_b32 s46, 0xc2ce8ed0
	v_cmp_ngt_f32_e32 vcc, s46, v4
	s_mov_b32 s89, 0x42b17218
	v_ldexp_f32 v5, v5, v8
	v_cndmask_b32_e32 v7, 0, v7, vcc
	v_cmp_ngt_f32_e32 vcc, s46, v3
	v_readlane_b32 s46, v254, 26
	s_cselect_b32 s58, s58, s46
	v_cndmask_b32_e32 v5, 0, v5, vcc
	v_cmp_nlt_f32_e32 vcc, s89, v3
	s_mulk_i32 s58, 0x1c00
	v_readlane_b32 s46, v254, 27
	v_cndmask_b32_e32 v3, v215, v5, vcc
	v_or_b32_e32 v5, s58, v6
	s_cselect_b32 s58, s60, s46
	s_mulk_i32 s58, 0x1c00
	v_readlane_b32 s46, v254, 28
	v_readlane_b32 s47, v254, 29
	v_or_b32_e32 v8, s58, v6
	s_cselect_b32 s58, s46, s47
	s_mulk_i32 s58, 0x1c00
	v_readlane_b32 s46, v254, 30
	v_readlane_b32 s47, v254, 31
	v_or_b32_e32 v9, s58, v6
	s_cselect_b32 s58, s46, s47
	s_mulk_i32 s58, 0x1c00
	v_readlane_b32 s46, v254, 32
	v_readlane_b32 s47, v254, 33
	v_or_b32_e32 v10, s58, v6
	s_cselect_b32 s58, s46, s47
	s_mulk_i32 s58, 0x1c00
	v_readlane_b32 s46, v254, 34
	v_readlane_b32 s47, v254, 35
	v_or_b32_e32 v11, s58, v6
	s_cselect_b32 s58, s46, s47
	s_mulk_i32 s58, 0x1c00
	v_readlane_b32 s46, v254, 36
	v_readlane_b32 s47, v254, 37
	v_or_b32_e32 v12, s58, v6
	s_cselect_b32 s58, s46, s47
	s_mulk_i32 s58, 0x1c00
	v_readlane_b32 s46, v254, 38
	v_readlane_b32 s47, v254, 39
	v_or_b32_e32 v13, s58, v6
	s_cselect_b32 s58, s46, s47
	s_mulk_i32 s58, 0x1c00
	v_add_f32_e32 v3, 1.0, v3
	v_or_b32_e32 v6, s58, v6
	v_lshlrev_b32_e32 v50, 1, v6
	v_div_scale_f32 v6, s[58:59], v3, v3, 1.0
	s_movk_i32 s58, 0x1800
	s_cselect_b32 s70, s58, 0x2000
	s_mov_b32 s58, 0x16600000
	s_cselect_b32 s58, s58, 0x1a600000
	s_add_u32 s82, s66, s58
	s_addc_u32 s83, s67, 0
	s_lshl_b32 s58, s5, 7
	s_and_b32 s88, s58, 0xfffff800
	s_and_b64 s[58:59], s[40:41], exec
	s_cselect_b32 s58, 0, 0x7c0
	s_or_b32 s58, s58, s88
	s_mul_hi_i32 s59, s58, 0x3800
	s_mulk_i32 s58, 0x3800
	s_add_u32 s86, s55, s58
	s_addc_u32 s87, s73, s59
	s_add_u32 s58, s86, s70
	s_addc_u32 s59, s87, 0
	s_add_u32 s84, s86, 0x1000
	s_addc_u32 s85, s87, 0
	v_lshlrev_b32_e32 v68, 1, v5
	s_add_u32 s86, s86, 0x2800
	v_lshlrev_b32_e32 v52, 1, v8
	v_lshlrev_b32_e32 v54, 1, v9
	v_lshlrev_b32_e32 v56, 1, v10
	v_lshlrev_b32_e32 v58, 1, v11
	v_lshlrev_b32_e32 v60, 1, v12
	v_lshlrev_b32_e32 v62, 1, v13
	s_addc_u32 s87, s87, 0
	global_load_dword v87, v68, s[58:59]
	global_load_dword v89, v68, s[84:85]
	global_load_dword v91, v68, s[86:87]
	global_load_dword v93, v52, s[58:59]
	global_load_dword v97, v52, s[84:85]
	global_load_dword v107, v52, s[86:87]
	global_load_dword v147, v54, s[84:85]
	global_load_dword v148, v54, s[86:87]
	global_load_dword v146, v54, s[58:59]
	global_load_dword v149, v56, s[58:59]
	global_load_dword v150, v56, s[84:85]
	global_load_dword v151, v56, s[86:87]
	global_load_dword v152, v58, s[58:59]
	global_load_dword v153, v58, s[84:85]
	global_load_dword v154, v58, s[86:87]
	global_load_dword v157, v60, s[86:87]
	global_load_dword v155, v60, s[58:59]
	global_load_dword v156, v60, s[84:85]
	global_load_dword v158, v62, s[58:59]
	global_load_dword v159, v62, s[84:85]
	global_load_dword v160, v62, s[86:87]
	global_load_dword v161, v50, s[58:59]
	global_load_dword v164, v50, s[84:85]
	global_load_dword v165, v50, s[86:87]
	v_rcp_f32_e32 v14, v6
	v_cmp_nlt_f32_e32 vcc, s89, v4
	v_readlane_b32 s46, v254, 40
	s_waitcnt lgkmcnt(0)
	v_fma_f32 v5, -v6, v14, 1.0
	v_cndmask_b32_e32 v4, v215, v7, vcc
	v_fmac_f32_e32 v14, v5, v14
	v_div_scale_f32 v5, vcc, 1.0, v3, 1.0
	v_mul_f32_e32 v7, v5, v14
	v_fma_f32 v8, -v6, v7, v5
	v_fmac_f32_e32 v7, v8, v14
	v_fma_f32 v5, -v6, v7, v5
	v_add_f32_e32 v4, 1.0, v4
	v_div_fmas_f32 v5, v5, v14, v7
	v_div_fixup_f32 v65, v5, v3, 1.0
	v_div_scale_f32 v3, s[58:59], v4, v4, 1.0
	v_rcp_f32_e32 v5, v3
	v_or_b32_e32 v6, s61, v189
	v_lshlrev_b32_e32 v6, 1, v6
	s_barrier
	v_fma_f32 v7, -v3, v5, 1.0
	v_fmac_f32_e32 v5, v7, v5
	v_div_scale_f32 v7, vcc, 1.0, v4, 1.0
	v_mul_f32_e32 v8, v7, v5
	v_fma_f32 v9, -v3, v8, v7
	v_fmac_f32_e32 v8, v9, v5
	v_fma_f32 v3, -v3, v8, v7
	v_div_fmas_f32 v3, v3, v5, v8
	v_div_fixup_f32 v64, v3, v4, 1.0
	v_cndmask_b32_e64 v3, v188, v187, s[40:41]
	v_lshlrev_b32_e32 v3, 11, v3
	v_mov_b32_e32 v2, 0
	v_or3_b32 v4, v6, s46, v3
	v_mov_b32_e32 v5, v69
	s_mov_b32 s89, 0
	v_pk_add_f32 v[108:109], v[64:65], 1.0 op_sel_hi:[1,0] neg_lo:[1,0] neg_hi:[1,0]
	v_mov_b32_e32 v53, v69
	v_mov_b32_e32 v55, v69
	v_mov_b32_e32 v57, v69
	v_mov_b32_e32 v59, v69
	v_mov_b32_e32 v61, v69
	v_mov_b32_e32 v63, v69
	v_mov_b32_e32 v51, v69
	v_lshl_add_u64 v[110:111], s[82:83], 0, v[4:5]
	s_movk_i32 s90, 0x780
	s_mov_b32 s91, 0
	v_mov_b32_e32 v3, v2
	v_mov_b32_e32 v4, v2
	v_mov_b32_e32 v5, v2
	v_mov_b32_e32 v6, v2
	v_mov_b32_e32 v7, v2
	v_mov_b32_e32 v8, v2
	v_mov_b32_e32 v9, v2
	v_mov_b32_e32 v10, v2
	v_mov_b32_e32 v11, v2
	v_mov_b32_e32 v12, v2
	v_mov_b32_e32 v13, v2
	v_mov_b32_e32 v14, v2
	v_mov_b32_e32 v15, v2
	v_mov_b32_e32 v16, v2
	v_mov_b32_e32 v17, v2
	v_mov_b32_e32 v18, v2
	v_mov_b32_e32 v19, v2
	v_mov_b32_e32 v20, v2
	v_mov_b32_e32 v21, v2
	v_mov_b32_e32 v22, v2
	v_mov_b32_e32 v23, v2
	v_mov_b32_e32 v24, v2
	v_mov_b32_e32 v25, v2
	v_mov_b32_e32 v26, v2
	v_mov_b32_e32 v27, v2
	v_mov_b32_e32 v28, v2
	v_mov_b32_e32 v29, v2
	v_mov_b32_e32 v30, v2
	v_mov_b32_e32 v31, v2
	v_mov_b32_e32 v32, v2
	v_mov_b32_e32 v33, v2
	v_readlane_b32 s92, v254, 11
	v_readlane_b32 s93, v254, 12
	v_and_b32_e32 v102, 3, v162
	v_bfe_u32 v103, v162, 2, 3
	v_lshrrev_b32_e32 v104, 5, v162
	v_lshlrev_b32_e32 v105, 16, v102
	v_lshl_or_b32 v105, v104, 18, v105
	v_lshl_or_b32 v105, v103, 4, v105
	v_and_b32_e32 v98, 1, v102
	v_lshlrev_b32_e32 v98, 18, v98
	v_lshrrev_b32_e32 v99, 1, v102
	v_lshl_or_b32 v99, v103, 1, v99
	v_lshl_or_b32 v98, v99, 11, v98
	v_lshl_or_b32 v103, v104, 4, v98
	v_mov_b32_e32 v102, v105
	v_mov_b32_e32 v104, 0x42000000
	v_mov_b32_e32 v105, 0x42000000
	s_and_b32 s46, s57, 3
	s_lshr_b32 s47, s57, 2
	s_lshl_b32 s68, s46, 19
	s_lshl_b32 s69, s47, 7
	s_or_b32 s68, s68, s69
	s_add_u32 s92, s92, s68
	s_addc_u32 s93, s93, 0
	s_lshl_b32 s68, s47, 15
	s_lshl_b32 s69, s46, 5
	s_or_b32 s68, s68, s69
	s_add_u32 s68, s68, 0x4ee00000
	s_add_u32 s94, s48, s68
	s_addc_u32 s95, s49, 0
	s_mov_b32 s46, 0
	s_mov_b64 s[96:97], s[92:93]
	global_load_dwordx4 v[70:73], v102, s[92:93] nt
	global_load_dwordx4 v[70:73], v102, s[92:93] nt
	global_load_dwordx4 v[70:73], v102, s[92:93] nt
	global_load_dwordx4 v[70:73], v102, s[92:93] nt
	global_load_dwordx4 v[70:73], v102, s[92:93] nt
	global_load_dwordx4 v[70:73], v102, s[92:93] nt
	global_load_dwordx4 v[70:73], v102, s[92:93] nt
	global_load_dwordx4 v[70:73], v102, s[92:93] nt
	s_branch .LBB0_357

.LBB0_357:
	s_waitcnt vmcnt(31)
	v_lshlrev_b32_e32 v34, 16, v87
	v_and_b32_e32 v35, 0xffff0000, v87
	v_mul_f32_e32 v34, 0xbfb8aa3b, v34
	v_mul_f32_e32 v35, 0xbfb8aa3b, v35
	v_exp_f32_e32 v34, v34
	v_exp_f32_e32 v35, v35
	s_waitcnt vmcnt(28)
	v_lshlrev_b32_e32 v36, 16, v93
	v_add_u32_e32 v167, 0, v190
	v_add_f32_e32 v34, 1.0, v34
	v_add_f32_e32 v35, 1.0, v35
	v_rcp_f32_e32 v34, v34
	v_rcp_f32_e32 v35, v35
	s_andn2_b64 vcc, exec, s[74:75]
	s_mov_b64 s[58:59], -1
	v_pk_mul_f32 v[120:121], v[108:109], v[34:35]
	v_and_b32_e32 v34, 0xffff0000, v93
	v_mul_f32_e32 v35, 0xbfb8aa3b, v36
	v_mul_f32_e32 v34, 0xbfb8aa3b, v34
	v_exp_f32_e32 v35, v35
	v_exp_f32_e32 v36, v34
	v_add_f32_e32 v37, v64, v120
	v_add_f32_e32 v38, v65, v121
	v_add_f32_e32 v34, 1.0, v35
	v_add_f32_e32 v35, 1.0, v36
	v_rcp_f32_e32 v34, v34
	v_rcp_f32_e32 v35, v35
	v_log_f32_e32 v36, v37
	v_log_f32_e32 v37, v38
	v_pk_mul_f32 v[122:123], v[108:109], v[34:35]
	s_waitcnt vmcnt(23)
	v_lshlrev_b32_e32 v34, 16, v146
	v_and_b32_e32 v35, 0xffff0000, v146
	v_mul_f32_e32 v34, 0xbfb8aa3b, v34
	v_mul_f32_e32 v35, 0xbfb8aa3b, v35
	v_exp_f32_e32 v34, v34
	v_exp_f32_e32 v35, v35
	v_add_f32_e32 v38, v64, v122
	v_add_f32_e32 v39, v65, v123
	v_add_f32_e32 v34, 1.0, v34
	v_add_f32_e32 v35, 1.0, v35
	v_rcp_f32_e32 v34, v34
	v_rcp_f32_e32 v35, v35
	v_log_f32_e32 v38, v38
	v_log_f32_e32 v39, v39
	v_pk_add_f32 v[144:145], v[36:37], 0 op_sel_hi:[1,0]
	v_pk_mul_f32 v[128:129], v[108:109], v[34:35]
	s_waitcnt vmcnt(22)
	v_lshlrev_b32_e32 v34, 16, v149
	v_and_b32_e32 v35, 0xffff0000, v149
	v_mul_f32_e32 v34, 0xbfb8aa3b, v34
	v_mul_f32_e32 v35, 0xbfb8aa3b, v35
	v_exp_f32_e32 v34, v34
	v_exp_f32_e32 v35, v35
	v_add_f32_e32 v40, v64, v128
	v_add_f32_e32 v41, v65, v129
	v_add_f32_e32 v34, 1.0, v34
	v_add_f32_e32 v35, 1.0, v35
	v_rcp_f32_e32 v34, v34
	v_rcp_f32_e32 v35, v35
	v_log_f32_e32 v40, v40
	v_log_f32_e32 v41, v41
	v_pk_add_f32 v[140:141], v[144:145], v[38:39]
	v_pk_mul_f32 v[126:127], v[108:109], v[34:35]
	s_waitcnt vmcnt(19)
	v_lshlrev_b32_e32 v34, 16, v152
	v_and_b32_e32 v35, 0xffff0000, v152
	v_mul_f32_e32 v34, 0xbfb8aa3b, v34
	v_mul_f32_e32 v35, 0xbfb8aa3b, v35
	v_exp_f32_e32 v34, v34
	v_exp_f32_e32 v35, v35
	v_add_f32_e32 v42, v64, v126
	v_add_f32_e32 v43, v65, v127
	v_add_f32_e32 v34, 1.0, v34
	v_add_f32_e32 v35, 1.0, v35
	v_rcp_f32_e32 v34, v34
	v_rcp_f32_e32 v35, v35
	v_log_f32_e32 v42, v42
	v_log_f32_e32 v43, v43
	v_pk_add_f32 v[136:137], v[140:141], v[40:41]
	v_pk_mul_f32 v[130:131], v[108:109], v[34:35]
	s_waitcnt vmcnt(15)
	v_lshlrev_b32_e32 v34, 16, v155
	v_and_b32_e32 v35, 0xffff0000, v155
	v_mul_f32_e32 v34, 0xbfb8aa3b, v34
	v_mul_f32_e32 v35, 0xbfb8aa3b, v35
	v_exp_f32_e32 v34, v34
	v_exp_f32_e32 v35, v35
	v_add_f32_e32 v44, v64, v130
	v_add_f32_e32 v45, v65, v131
	v_add_f32_e32 v34, 1.0, v34
	v_add_f32_e32 v35, 1.0, v35
	v_rcp_f32_e32 v34, v34
	v_rcp_f32_e32 v35, v35
	v_log_f32_e32 v44, v44
	v_log_f32_e32 v45, v45
	v_pk_add_f32 v[132:133], v[136:137], v[42:43]
	v_pk_mul_f32 v[134:135], v[108:109], v[34:35]
	s_waitcnt vmcnt(13)
	v_lshlrev_b32_e32 v34, 16, v158
	v_and_b32_e32 v35, 0xffff0000, v158
	v_mul_f32_e32 v34, 0xbfb8aa3b, v34
	v_mul_f32_e32 v35, 0xbfb8aa3b, v35
	v_exp_f32_e32 v34, v34
	v_exp_f32_e32 v35, v35
	v_add_f32_e32 v46, v64, v134
	v_add_f32_e32 v47, v65, v135
	v_add_f32_e32 v34, 1.0, v34
	v_add_f32_e32 v35, 1.0, v35
	v_rcp_f32_e32 v34, v34
	v_rcp_f32_e32 v35, v35
	v_log_f32_e32 v46, v46
	v_log_f32_e32 v47, v47
	v_pk_add_f32 v[124:125], v[132:133], v[44:45]
	v_pk_mul_f32 v[138:139], v[108:109], v[34:35]
	s_waitcnt vmcnt(10)
	v_lshlrev_b32_e32 v34, 16, v161
	v_and_b32_e32 v35, 0xffff0000, v161
	v_mul_f32_e32 v34, 0xbfb8aa3b, v34
	v_mul_f32_e32 v35, 0xbfb8aa3b, v35
	v_exp_f32_e32 v34, v34
	v_exp_f32_e32 v35, v35
	v_add_f32_e32 v48, v64, v138
	v_add_f32_e32 v49, v65, v139
	v_add_f32_e32 v34, 1.0, v34
	v_add_f32_e32 v35, 1.0, v35
	v_rcp_f32_e32 v34, v34
	v_rcp_f32_e32 v35, v35
	v_log_f32_e32 v48, v48
	v_log_f32_e32 v49, v49
	v_pk_add_f32 v[118:119], v[124:125], v[46:47]
	v_pk_mul_f32 v[142:143], v[108:109], v[34:35]
	v_and_b32_e32 v36, 0xffff, v154
	v_add_f32_e32 v34, v64, v142
	v_add_f32_e32 v35, v65, v143
	v_log_f32_e32 v34, v34
	v_log_f32_e32 v35, v35
	v_pk_add_f32 v[114:115], v[118:119], v[48:49]
	v_and_b32_e32 v37, 0xffff, v160
	v_lshl_or_b32 v36, v157, 16, v36
	v_pk_add_f32 v[112:113], v[114:115], v[34:35]
	v_add_u32_e32 v34, s63, v190
	ds_write_b64 v34, v[112:113]
	v_and_b32_e32 v34, 0xffff, v91
	v_and_b32_e32 v35, 0xffff, v148
	v_lshl_or_b32 v34, v107, 16, v34
	v_lshl_or_b32 v35, v151, 16, v35
	s_waitcnt vmcnt(8)
	v_lshl_or_b32 v37, v165, 16, v37
	v_lshrrev_b32_e32 v38, 16, v91
	v_lshrrev_b32_e32 v39, 16, v148
	v_lshrrev_b32_e32 v40, 16, v154
	v_lshrrev_b32_e32 v41, 16, v160
	v_add_u32_e32 v42, s64, v191
	v_and_or_b32 v38, v107, s53, v38
	v_and_or_b32 v39, v151, s53, v39
	v_and_or_b32 v40, v157, s53, v40
	v_and_or_b32 v41, v165, s53, v41
	ds_write_b128 v42, v[34:37] offset:53248
	ds_write_b128 v42, v[38:41] offset:53392
	s_waitcnt lgkmcnt(0)
	s_barrier
	v_add_u32_e32 v34, 0x24c00, v167
	ds_read2st64_b64 v[46:49], v34 offset1:1
	ds_read2st64_b64 v[42:45], v34 offset0:2 offset1:3
	ds_read2st64_b64 v[38:41], v34 offset0:4 offset1:5
	ds_read2st64_b64 v[34:37], v34 offset0:6 offset1:7
	s_waitcnt lgkmcnt(3)
	v_add_f32_e32 v166, 0, v46
	v_add_f32_e32 v46, v166, v48
	s_waitcnt lgkmcnt(2)
	v_add_f32_e32 v46, v46, v42
	v_add_f32_e32 v46, v46, v44
	s_waitcnt lgkmcnt(1)
	v_add_f32_e32 v46, v46, v38
	v_add_f32_e32 v46, v46, v40
	s_waitcnt lgkmcnt(0)
	v_add_f32_e32 v46, v46, v34
	v_add_f32_e32 v46, v46, v36
	v_exp_f32_e32 v116, v46
	s_cbranch_vccnz .LBB0_359
	s_mov_b64 s[58:59], 0

.LBB0_361:
	v_cndmask_b32_e64 v47, v47, 0, s[44:45]
	v_cndmask_b32_e64 v166, v166, 0, s[44:45]
	v_add_f32_e32 v48, v48, v166
	v_add_f32_e32 v49, v49, v47
	v_cndmask_b32_e64 v47, v47, v49, s[8:9]
	v_cndmask_b32_e64 v48, v166, v48, s[8:9]
	v_add_f32_e32 v42, v42, v48
	v_add_f32_e32 v43, v43, v47
	v_cndmask_b32_e64 v43, v47, v43, s[10:11]
	v_cndmask_b32_e64 v42, v48, v42, s[10:11]
	v_add_f32_e32 v44, v44, v42
	v_add_f32_e32 v45, v45, v43
	v_cndmask_b32_e64 v43, v43, v45, s[12:13]
	v_cndmask_b32_e64 v42, v42, v44, s[12:13]
	v_add_f32_e32 v38, v38, v42
	v_add_f32_e32 v39, v39, v43
	v_cndmask_b32_e64 v39, v43, v39, s[14:15]
	v_cndmask_b32_e64 v38, v42, v38, s[14:15]
	v_add_f32_e32 v40, v40, v38
	v_add_f32_e32 v41, v41, v39
	v_cndmask_b32_e64 v39, v39, v41, s[16:17]
	v_cndmask_b32_e64 v38, v38, v40, s[16:17]
	v_add_f32_e32 v34, v34, v38
	v_add_f32_e32 v35, v35, v39
	v_cndmask_b32_e64 v35, v39, v35, s[18:19]
	v_cndmask_b32_e64 v34, v38, v34, s[18:19]
	v_add_f32_e32 v36, v36, v34
	v_add_f32_e32 v37, v37, v35
	v_cndmask_b32_e64 v47, v35, v37, s[20:21]
	v_cndmask_b32_e64 v166, v34, v36, s[20:21]
	v_add_f32_e32 v34, v144, v166
	v_add_f32_e32 v35, v145, v47
	v_exp_f32_e32 v34, v34
	v_exp_f32_e32 v35, v35
	v_pk_add_f32 v[120:121], v[108:109], v[120:121] neg_lo:[0,1] neg_hi:[0,1]
	v_pk_add_f32 v[36:37], v[108:109], v[126:127] neg_lo:[0,1] neg_hi:[0,1]
	v_rcp_f32_e32 v40, v34
	v_rcp_f32_e32 v41, v35
	v_add_f32_e32 v126, v140, v166
	v_add_f32_e32 v127, v141, v47
	v_exp_f32_e32 v126, v126
	v_pk_mul_f32 v[40:41], v[120:121], v[40:41]
	v_lshlrev_b32_e32 v120, 16, v89
	v_and_b32_e32 v121, 0xffff0000, v89
	v_exp_f32_e32 v127, v127
	v_pk_mul_f32 v[34:35], v[34:35], v[120:121]
	s_mul_i32 s58, s57, 0x880
	v_pk_add_f32 v[38:39], v[108:109], v[130:131] neg_lo:[0,1] neg_hi:[0,1]
	v_cvt_pk_bf16_f32 v120, v34, v35
	v_add_u32_e32 v121, s58, v192
	v_cvt_pk_bf16_f32 v130, v40, v41
	ds_write2st64_b32 v121, v120, v130 offset1:68
	v_lshlrev_b32_e32 v120, 16, v97
	v_and_b32_e32 v121, 0xffff0000, v97
	v_pk_mul_f32 v[120:121], v[126:127], v[120:121]
	v_rcp_f32_e32 v34, v126
	v_cvt_pk_bf16_f32 v130, v120, v121
	v_add_f32_e32 v120, v136, v166
	v_add_f32_e32 v121, v137, v47
	v_exp_f32_e32 v120, v120
	v_exp_f32_e32 v121, v121
	v_rcp_f32_e32 v35, v127
	v_pk_add_f32 v[122:123], v[108:109], v[122:123] neg_lo:[0,1] neg_hi:[0,1]
	v_rcp_f32_e32 v126, v120
	v_rcp_f32_e32 v127, v121
	v_pk_mul_f32 v[34:35], v[122:123], v[34:35]
	v_pk_add_f32 v[128:129], v[108:109], v[128:129] neg_lo:[0,1] neg_hi:[0,1]
	v_pk_add_f32 v[42:43], v[108:109], v[134:135] neg_lo:[0,1] neg_hi:[0,1]
	v_cvt_pk_bf16_f32 v134, v34, v35
	v_mov_b32_e32 v123, v34
	v_mov_b32_e32 v34, v41
	v_mov_b32_e32 v122, v40
	v_pk_mul_f32 v[40:41], v[46:47], v[34:35] op_sel_hi:[0,1]
	v_pk_mul_f32 v[34:35], v[128:129], v[126:127]
	v_lshlrev_b32_e32 v126, 16, v147
	v_and_b32_e32 v127, 0xffff0000, v147
	v_pk_mul_f32 v[120:121], v[120:121], v[126:127]
	v_add_f32_e32 v126, v132, v166
	v_add_f32_e32 v127, v133, v47
	v_exp_f32_e32 v126, v126
	v_exp_f32_e32 v127, v127
	s_mul_i32 s58, s60, 0x110
	v_add_u32_e32 v131, s58, v192
	v_cvt_pk_bf16_f32 v120, v120, v121
	ds_write2_b32 v131, v130, v120 offset1:68
	v_rcp_f32_e32 v120, v126
	v_rcp_f32_e32 v121, v127
	v_cvt_pk_bf16_f32 v128, v34, v35
	v_add_u32_e32 v130, 0x4400, v131
	ds_write2_b32 v130, v134, v128 offset1:68
	v_pk_mul_f32 v[36:37], v[36:37], v[120:121]
	v_lshlrev_b32_e32 v120, 16, v150
	v_and_b32_e32 v121, 0xffff0000, v150
	v_pk_mul_f32 v[120:121], v[126:127], v[120:121]
	v_cvt_pk_bf16_f32 v133, v36, v37
	v_cvt_pk_bf16_f32 v132, v120, v121
	v_add_f32_e32 v120, v124, v166
	v_add_f32_e32 v121, v125, v47
	v_exp_f32_e32 v120, v120
	v_exp_f32_e32 v121, v121
	v_mov_b32_e32 v124, v34
	v_mov_b32_e32 v125, v36
	v_rcp_f32_e32 v126, v120
	v_rcp_f32_e32 v127, v121
	v_mov_b32_e32 v36, v35
	v_pk_mul_f32 v[128:129], v[46:47], v[36:37] op_sel_hi:[0,1]
	v_lshlrev_b32_e32 v36, 16, v153
	v_pk_mul_f32 v[34:35], v[38:39], v[126:127]
	v_add_f32_e32 v38, v118, v166
	v_add_f32_e32 v39, v119, v47
	v_exp_f32_e32 v38, v38
	v_exp_f32_e32 v39, v39
	v_and_b32_e32 v37, 0xffff0000, v153
	v_pk_mul_f32 v[36:37], v[120:121], v[36:37]
	v_pk_add_f32 v[44:45], v[108:109], v[138:139] neg_lo:[0,1] neg_hi:[0,1]
	v_cvt_pk_bf16_f32 v118, v36, v37
	v_rcp_f32_e32 v36, v38
	v_rcp_f32_e32 v37, v39
	ds_write2_b32 v131, v132, v118 offset0:136 offset1:204
	v_cvt_pk_bf16_f32 v118, v34, v35
	ds_write2_b32 v130, v133, v118 offset0:136 offset1:204
	v_pk_mul_f32 v[36:37], v[42:43], v[36:37]
	v_lshlrev_b32_e32 v42, 16, v156
	v_and_b32_e32 v43, 0xffff0000, v156
	v_pk_mul_f32 v[38:39], v[38:39], v[42:43]
	v_cvt_pk_bf16_f32 v121, v36, v37
	v_cvt_pk_bf16_f32 v120, v38, v39
	v_add_f32_e32 v38, v114, v166
	v_add_f32_e32 v39, v115, v47
	v_exp_f32_e32 v38, v38
	v_exp_f32_e32 v39, v39
	v_mov_b32_e32 v43, v36
	v_mov_b32_e32 v36, v35
	v_pk_mul_f32 v[118:119], v[46:47], v[36:37] op_sel_hi:[0,1]
	v_lshlrev_b32_e32 v36, 16, v159
	v_and_b32_e32 v37, 0xffff0000, v159
	v_pk_mul_f32 v[36:37], v[38:39], v[36:37]
	v_rcp_f32_e32 v114, v38
	v_cvt_pk_bf16_f32 v38, v36, v37
	v_add_f32_e32 v36, v112, v166
	v_add_f32_e32 v37, v113, v47
	v_rcp_f32_e32 v115, v39
	v_exp_f32_e32 v36, v36
	v_exp_f32_e32 v37, v37
	v_add_u32_e32 v39, 0x400, v131
	v_mov_b32_e32 v42, v34
	v_pk_mul_f32 v[34:35], v[44:45], v[114:115]
	ds_write2_b32 v39, v120, v38 offset0:16 offset1:84
	v_rcp_f32_e32 v38, v36
	v_rcp_f32_e32 v39, v37
	v_cvt_pk_bf16_f32 v44, v34, v35
	v_add_u32_e32 v45, 0x4800, v131
	ds_write2_b32 v45, v121, v44 offset0:16 offset1:84
	v_lshlrev_b32_e32 v44, 16, v164
	v_and_b32_e32 v45, 0xffff0000, v164
	v_pk_add_f32 v[48:49], v[108:109], v[142:143] neg_lo:[0,1] neg_hi:[0,1]
	v_pk_mul_f32 v[36:37], v[36:37], v[44:45]
	v_pk_mul_f32 v[38:39], v[48:49], v[38:39]
	v_cvt_pk_bf16_f32 v36, v36, v37
	ds_write_b32 v131, v36 offset:1632
	v_cvt_pk_bf16_f32 v36, v38, v39
	ds_write_b32 v131, v36 offset:19040
	v_mov_b32_e32 v36, v34
	v_mov_b32_e32 v37, v38
	v_pk_mul_f32 v[122:123], v[116:117], v[122:123] op_sel_hi:[0,1]
	v_pk_mul_f32 v[124:125], v[116:117], v[124:125] op_sel_hi:[0,1]
	v_pk_mul_f32 v[42:43], v[116:117], v[42:43] op_sel_hi:[0,1]
	v_pk_mul_f32 v[44:45], v[116:117], v[36:37] op_sel_hi:[0,1]
	v_mov_b32_e32 v38, v35
	v_pk_mul_f32 v[38:39], v[46:47], v[38:39] op_sel_hi:[0,1]
	v_cvt_pk_bf16_f32 v34, v122, v123
	v_cvt_pk_bf16_f32 v35, v124, v125
	v_cvt_pk_bf16_f32 v36, v42, v43
	v_cvt_pk_bf16_f32 v37, v44, v45
	ds_write_b128 v204, v[34:37] offset:34816
	v_cvt_pk_bf16_f32 v34, v40, v41
	v_cvt_pk_bf16_f32 v35, v128, v129
	v_cvt_pk_bf16_f32 v36, v118, v119
	v_cvt_pk_bf16_f32 v37, v38, v39
	s_sub_u32 s47, s46, 1
	s_cmp_lt_u32 s47, 28
	s_cbranch_scc0 .Lhg_skipC
	s_waitcnt vmcnt(4)
	v_pk_mul_f32 v[70:71], v[70:71], v[104:105]
	v_pk_mul_f32 v[72:73], v[72:73], v[104:105]
	v_pk_mul_f32 v[74:75], v[74:75], v[104:105]
	v_pk_mul_f32 v[76:77], v[76:77], v[104:105]
	v_pk_mul_f32 v[78:79], v[78:79], v[104:105]
	v_pk_mul_f32 v[80:81], v[80:81], v[104:105]
	v_pk_mul_f32 v[82:83], v[82:83], v[104:105]
	v_pk_mul_f32 v[84:85], v[84:85], v[104:105]
	v_cvt_pk_fp8_f32 v70, v70, v74
	v_cvt_pk_fp8_f32 v71, v71, v75
	v_cvt_pk_fp8_f32 v72, v72, v76
	v_cvt_pk_fp8_f32 v73, v73, v77
	v_cvt_pk_fp8_f32 v70, v78, v82 op_sel:[0,0,1]
	v_cvt_pk_fp8_f32 v71, v79, v83 op_sel:[0,0,1]
	v_cvt_pk_fp8_f32 v72, v80, v84 op_sel:[0,0,1]
	v_cvt_pk_fp8_f32 v73, v81, v85 op_sel:[0,0,1]
	s_mov_b32 vcc_lo, 0xaaaaaaaa
	s_mov_b32 vcc_hi, 0xaaaaaaaa
	s_nop 1
	v_cndmask_b32_dpp v75, v70, v71, vcc quad_perm:[1,0,3,2] row_mask:0xf bank_mask:0xf
	v_cndmask_b32_dpp v77, v72, v73, vcc quad_perm:[1,0,3,2] row_mask:0xf bank_mask:0xf
	s_not_b64 vcc, vcc
	v_cndmask_b32_dpp v74, v71, v70, vcc quad_perm:[1,0,3,2] row_mask:0xf bank_mask:0xf
	v_cndmask_b32_dpp v76, v73, v72, vcc quad_perm:[1,0,3,2] row_mask:0xf bank_mask:0xf
	s_mov_b32 vcc_lo, 0xcccccccc
	s_mov_b32 vcc_hi, 0xcccccccc
	s_nop 1
	v_cndmask_b32_dpp v100, v74, v76, vcc quad_perm:[2,3,0,1] row_mask:0xf bank_mask:0xf
	v_cndmask_b32_dpp v101, v75, v77, vcc quad_perm:[2,3,0,1] row_mask:0xf bank_mask:0xf
	s_not_b64 vcc, vcc
	v_cndmask_b32_dpp v98, v76, v74, vcc quad_perm:[2,3,0,1] row_mask:0xf bank_mask:0xf
	v_cndmask_b32_dpp v99, v77, v75, vcc quad_perm:[2,3,0,1] row_mask:0xf bank_mask:0xf
	global_store_dwordx4 v103, v[98:101], s[42:43] nt
.Lhg_skipC:
	s_cmpk_eq_i32 s90, 0xffc0
	ds_write_b128 v204, v[34:37] offset:34960
	s_cbranch_scc1 .LBB0_363
	s_add_i32 s61, s89, 64
	s_and_b64 s[58:59], s[40:41], exec
	s_cselect_b32 s58, s61, s90
	s_add_i32 s58, s58, s88
	s_mul_hi_i32 s59, s58, 0x3800
	s_mulk_i32 s58, 0x3800
	s_add_u32 s58, s55, s58
	s_addc_u32 s59, s73, s59
	s_add_u32 s86, s58, s70
	s_addc_u32 s87, s59, 0
	s_add_u32 s84, s58, 0x1000
	s_addc_u32 s85, s59, 0
	s_add_u32 s82, s58, 0x2800
	v_lshl_add_u64 v[34:35], s[86:87], 0, v[68:69]
	s_addc_u32 s83, s59, 0
	global_load_dword v87, v[34:35], off
	v_lshl_add_u64 v[34:35], s[84:85], 0, v[68:69]
	global_load_dword v89, v[34:35], off
	v_lshl_add_u64 v[34:35], s[82:83], 0, v[68:69]
	global_load_dword v91, v[34:35], off
	v_lshl_add_u64 v[34:35], s[86:87], 0, v[52:53]
	global_load_dword v93, v[34:35], off
	v_lshl_add_u64 v[34:35], s[84:85], 0, v[52:53]
	global_load_dword v97, v[34:35], off
	v_lshl_add_u64 v[34:35], s[82:83], 0, v[52:53]
	global_load_dword v107, v[34:35], off
	v_lshl_add_u64 v[34:35], s[86:87], 0, v[54:55]
	global_load_dword v146, v[34:35], off
	v_lshl_add_u64 v[34:35], s[84:85], 0, v[54:55]
	global_load_dword v147, v[34:35], off
	v_lshl_add_u64 v[34:35], s[82:83], 0, v[54:55]
	global_load_dword v148, v[34:35], off
	v_lshl_add_u64 v[34:35], s[86:87], 0, v[56:57]
	global_load_dword v149, v[34:35], off
	v_lshl_add_u64 v[34:35], s[84:85], 0, v[56:57]
	global_load_dword v150, v[34:35], off
	v_lshl_add_u64 v[34:35], s[82:83], 0, v[56:57]
	global_load_dword v151, v[34:35], off
	v_lshl_add_u64 v[34:35], s[86:87], 0, v[58:59]
	global_load_dword v152, v[34:35], off
	v_lshl_add_u64 v[34:35], s[84:85], 0, v[58:59]
	global_load_dword v153, v[34:35], off
	v_lshl_add_u64 v[34:35], s[82:83], 0, v[58:59]
	global_load_dword v154, v[34:35], off
	v_lshl_add_u64 v[34:35], s[86:87], 0, v[60:61]
	global_load_dword v155, v[34:35], off
	v_lshl_add_u64 v[34:35], s[84:85], 0, v[60:61]
	global_load_dword v156, v[34:35], off
	v_lshl_add_u64 v[34:35], s[82:83], 0, v[60:61]
	global_load_dword v157, v[34:35], off
	v_lshl_add_u64 v[34:35], s[86:87], 0, v[62:63]
	global_load_dword v158, v[34:35], off
	v_lshl_add_u64 v[34:35], s[84:85], 0, v[62:63]
	global_load_dword v159, v[34:35], off
	v_lshl_add_u64 v[34:35], s[82:83], 0, v[62:63]
	global_load_dword v160, v[34:35], off
	v_lshl_add_u64 v[34:35], s[86:87], 0, v[50:51]
	global_load_dword v161, v[34:35], off
	v_lshl_add_u64 v[34:35], s[84:85], 0, v[50:51]
	global_load_dword v164, v[34:35], off
	v_lshl_add_u64 v[34:35], s[82:83], 0, v[50:51]
	global_load_dword v165, v[34:35], off
	s_cmp_lt_u32 s46, 28
	s_cbranch_scc0 .Lhg_skipL
	s_lshr_b32 s47, s46, 2
	s_lshl_b32 s47, s47, 7
	s_add_u32 s47, s47, s5
	s_add_u32 s47, s47, 6016
	s_and_b32 s68, s46, 3
	s_lshr_b32 s69, s47, 4
	s_lshl_b32 s69, s69, 21
	s_and_b32 s0, s47, 15
	s_lshl_b32 s1, s0, 10
	s_or_b32 s69, s69, s1
	s_lshl_b32 s1, s68, 8
	s_or_b32 s69, s69, s1
	s_add_u32 s96, s92, s69
	s_addc_u32 s97, s93, 0
	s_lshr_b32 s69, s47, 8
	s_lshl_b32 s69, s69, 23
	s_lshl_b32 s0, s0, 19
	s_or_b32 s69, s69, s0
	s_bfe_u32 s0, s47, 0x40004
	s_lshl_b32 s0, s0, 7
	s_or_b32 s69, s69, s0
	s_lshl_b32 s0, s68, 16
	s_or_b32 s69, s69, s0
	s_add_u32 s42, s94, s69
	s_addc_u32 s43, s95, 0
.Lhg_skipL:
	global_load_dwordx4 v[70:73], v102, s[96:97] nt
	s_add_u32 s96, s96, 0x4000
	s_addc_u32 s97, s97, 0
	global_load_dwordx4 v[74:77], v102, s[96:97] nt
	s_add_u32 s96, s96, 0x4000
	s_addc_u32 s97, s97, 0
	global_load_dwordx4 v[78:81], v102, s[96:97] nt
	s_add_u32 s96, s96, 0x4000
	s_addc_u32 s97, s97, 0
	global_load_dwordx4 v[82:85], v102, s[96:97] nt
	s_add_u32 s46, s46, 1
